# MoE M3: one agent-scope acquire per workgroup and unit (wave 0 invalidates + waits, the others pass a workgroup barrier before their loads) instead of eight per-wave invalidates; arrival-time barrier
# baseline (speedup 1.0000x reference)
.LBB0_1254:
	v_readlane_b32 s100, v254, 9
	s_nop 0
	s_cmp_lg_u32 s100, 0
	s_cbranch_scc1 .Lm3acq_first
	s_mov_b64 s[100:101], exec
	s_mov_b64 exec, -1
	buffer_inv sc1
	s_waitcnt vmcnt(0)
	s_mov_b64 exec, s[100:101]
.Lm3acq_first:
	s_barrier
	s_lshl_b32 s10, s12, 4
	s_add_u32 s2, s8, 0x59140000
	s_addc_u32 s3, s9, 0
	s_lshl_b32 s50, s90, 25
	s_lshl_b64 s[14:15], s[50:51], 2
	s_add_u32 s16, s6, s14
	s_addc_u32 s17, s7, s15
	v_and_b32_e32 v3, 60, v206
	s_add_i32 s22, 0, 0x24200
	v_add_u32_e32 v200, s22, v3
	v_ashrrev_i32_e32 v3, 2, v206
	v_and_b32_e32 v201, -16, v3
	v_lshl_add_u32 v3, v201, 2, v200
	ds_read_b32 v3, v3
	v_add_u32_e32 v7, 0x2000, v4
	v_ashrrev_i32_e32 v7, 6, v7
	v_and_b32_e32 v202, -16, v7
	v_lshl_add_u32 v7, v202, 2, v200
	s_ashr_i32 s6, s5, 6
	ds_read_b32 v7, v7
	s_lshl_b32 s13, s6, 10
	s_waitcnt lgkmcnt(1)
	v_max_i32_e32 v3, 0, v3
	v_and_b32_e32 v5, 32, v206
	v_and_b32_e32 v8, 48, v4
	v_lshlrev_b32_e32 v3, 10, v3
	s_add_i32 s13, s13, 0
	s_ashr_i32 s18, s5, 8
	s_and_b32 s19, s5, 0xc0
	v_bitop3_b32 v220, v3, v8, v5 bitop3:0xf6
	s_ashr_i32 s5, s4, 31
	s_mov_b32 m0, s13
	s_lshl_b32 s11, s18, 13
	s_lshl_b64 s[4:5], s[4:5], 22
	s_ashr_i32 s7, s6, 31
	global_load_lds_dwordx4 v220, s[2:3]
	s_add_i32 m0, s13, 0x2000
	s_waitcnt lgkmcnt(0)
	v_max_i32_e32 v3, 0, v7
	s_add_u32 s14, s16, s4
	v_lshlrev_b32_e32 v3, 10, v3
	v_lshlrev_b32_e32 v2, 8, v2
	s_addc_u32 s15, s17, s5
	s_lshl_b64 s[4:5], s[6:7], 13
	v_and_b32_e32 v1, 63, v206
	v_bitop3_b32 v221, v3, v8, v5 bitop3:0xf6
	v_ashrrev_i32_e32 v3, 31, v2
	s_add_u32 s6, s14, s4
	v_lshlrev_b32_e32 v0, 2, v1
	s_addc_u32 s7, s15, s5
	v_lshlrev_b64 v[2:3], 2, v[2:3]
	v_xor_b32_e32 v6, 16, v0
	v_lshl_add_u64 v[2:3], s[6:7], 0, v[2:3]
	global_load_lds_dwordx4 v221, s[2:3]
	v_lshlrev_b32_e32 v208, 4, v1
	v_lshlrev_b32_e32 v8, 2, v6
	v_mov_b32_e32 v9, v209
	s_add_i32 m0, s13, 0x4000
	v_readfirstlane_b32 s6, v2
	v_readfirstlane_b32 s7, v3
	v_lshl_add_u64 v[198:199], v[2:3], 0, v[8:9]
	v_lshl_add_u64 v[196:197], v[2:3], 0, v[208:209]
	v_or_b32_e32 v1, 64, v220
	v_lshlrev_b32_e32 v7, 2, v206
	v_and_b32_e32 v7, 32, v7
	global_load_lds_dwordx4 v208, s[6:7]
	s_mov_b64 s[6:7], 0x10000
	v_lshl_add_u64 v[2:3], v[198:199], 0, s[6:7]
	s_add_i32 m0, s13, 0x6000
	s_mov_b64 s[6:7], 0x20000
	global_load_lds_dwordx4 v[2:3], off
	v_lshl_add_u64 v[2:3], v[196:197], 0, s[6:7]
	s_add_i32 m0, s13, 0x8000
	s_mov_b64 s[6:7], 0x30000
	global_load_lds_dwordx4 v[2:3], off
	v_lshl_add_u64 v[2:3], v[198:199], 0, s[6:7]
	s_add_i32 m0, s13, 0xa000
	s_mov_b64 s[6:7], 0x40000
	global_load_lds_dwordx4 v[2:3], off
	s_add_i32 m0, s13, 0xc000
	v_lshl_add_u64 v[2:3], v[196:197], 0, s[6:7]
	global_load_lds_dwordx4 v1, s[2:3]
	v_or_b32_e32 v1, 64, v221
	s_add_i32 m0, s13, 0xe000
	s_mov_b64 s[6:7], 0x50000
	global_load_lds_dwordx4 v1, s[2:3]
	s_add_i32 m0, s13, 0x10000
	v_and_b32_e32 v1, 15, v206
	global_load_lds_dwordx4 v[2:3], off
	v_lshl_add_u64 v[2:3], v[198:199], 0, s[6:7]
	s_add_i32 m0, s13, 0x12000
	s_mov_b64 s[6:7], 0x60000
	global_load_lds_dwordx4 v[2:3], off
	v_lshl_add_u64 v[2:3], v[196:197], 0, s[6:7]
	s_add_i32 m0, s13, 0x14000
	s_mov_b64 s[6:7], 0x70000
	global_load_lds_dwordx4 v[2:3], off
	v_lshl_add_u64 v[2:3], v[198:199], 0, s[6:7]
	s_add_i32 m0, s13, 0x16000
	s_add_u32 s16, s16, s4
	global_load_lds_dwordx4 v[2:3], off
	v_lshlrev_b32_e32 v3, 6, v1
	v_and_b32_e32 v2, 48, v206
	v_bitop3_b32 v203, v3, v7, v2 bitop3:0x36
	v_lshlrev_b32_e32 v3, 1, v1
	v_and_b32_e32 v7, 16, v206
	s_addc_u32 s17, s17, s5
	s_lshl_b32 s7, s18, 9
	s_lshl_b32 s4, s19, 1
	v_bitop3_b32 v3, s19, v7, v3 bitop3:0x36
	s_add_u32 s4, s8, s4
	v_lshlrev_b32_e32 v205, 2, v3
	s_addc_u32 s5, s9, 0
	v_mov_b32_e32 v3, v209
	v_lshlrev_b32_e32 v7, 9, v206
	v_lshl_add_u64 v[2:3], s[4:5], 0, v[2:3]
	s_mov_b64 s[4:5], 0x5a140000
	s_add_i32 s22, s22, s7
	s_mov_b32 s6, 2
	s_mov_b32 s14, 16
	v_and_b32_e32 v204, 0x6000, v7
	v_bitop3_b32 v206, v4, v5, 48 bitop3:0x6c
	s_mov_b32 s15, 0
	v_lshl_add_u64 v[192:193], v[2:3], 0, s[4:5]
	v_lshl_add_u32 v207, v1, 2, s22
	v_lshlrev_b32_e32 v208, 2, v0
	v_lshlrev_b32_e32 v194, 2, v6
	s_mov_b32 s18, 2
	s_mov_b32 s19, 2
	s_mov_b32 s22, 0
	s_mov_b32 s23, 0
	s_mov_b32 s24, 0
	s_branch .LBB0_1256
